# v16 + attention unit end: store drain before the LDS-release barrier removed; next unit's first K/V tiles prefetched into L2 from the unit tail (diff + MLA)
# baseline (speedup 1.0000x reference)
; __device__ __forceinline__ void diff_attn_phase(Frame& F, const InPtrs& A, bool do_ctx, int conv_layer) {
;     ...
;     for (int u = F.vcu; u < nunits; u += F.G) {
;         const bool lat = u < 2048; const int bh = lat ? (u >> 4) : (u - 2048), qb = lat ? (u & 15) : 0, b = bh >> 4, vh = bh & 15, h = vh >> 1;
;         const bf16* Qp = lat ? DQ + ((size_t)bh * 4096 + qb * 256) * 64 : DQC + (size_t)bh * 256 * 64;
;         const bf16* Kp = DKp + (size_t)bh * NKEYS * 64;
;         const bf16* V0 = QKV + (size_t)(NLAT + b * 256) * 3072 + 2048 + h * 128; const bf16* V1 = QKV + (size_t)(b * 4096) * 3072 + 2048 + h * 128;
;         bf16* Op = OB + (size_t)(lat ? b * 4096 + qb * 256 : NLAT + b * 256) * 2048 + vh * 128;
;         const att::QLoadPlain QL{Qp, 64};
;         if (!use_off) att::body_dma<64, 128, false>(QL, Kp, Kp + 256 * 64, 64, V0, V1, 3072, Op, 2048, lat ? NKEYS : 256, 0.f, (char*)F.lds, F.tid);
;         else { int bi_ = __builtin_amdgcn_readfirstlane(__builtin_bit_cast(int, bound)); asm volatile("" : "+s"(bi_)); const float nm_ = -fminf(__builtin_bit_cast(float, bi_), 30.0f) * 1.4426950408889634f;     att::body<64, 128, 1, true>(QL, Kp, Kp + 256 * 64, 64, V0, V1, 3072, Op, 2048, lat ? NKEYS : 256, nm_, (char*)F.lds, F.tid); }
.LBB0_918:
	s_add_i32 s80, s73, s51
	s_cmpk_ge_i32 s80, 0x800
	s_cbranch_scc1 .Lpf_d_skip
	s_add_u32 s76, s16, 0x880000
	s_addc_u32 s77, s17, 0
	s_add_u32 s78, s18, 0x180000
	s_addc_u32 s79, s19, 0
	v_readlane_b32 s80, v251, 12
	v_mbcnt_lo_u32_b32 v240, -1, 0
	v_mbcnt_hi_u32_b32 v240, -1, v240
	v_add_u32_e32 v240, s80, v240
	v_lshlrev_b32_e32 v241, 7, v240
	global_load_dword v242, v241, s[76:77]
	v_lshrrev_b32_e32 v241, 1, v240
	v_mul_u32_u24_e32 v241, 0x1800, v241
	v_and_b32_e32 v243, 1, v240
	v_lshl_add_u32 v241, v243, 7, v241
	global_load_dword v244, v241, s[78:79]

; __device__ __forceinline__ void mla_attn_phase(Frame& F, const InPtrs& A, int jl, bool do_ctx, int conv_layer) {
;     ...
;     for (int u = F.vcu; u < nunits; u += F.G) {
;         const bool lat = u < 2048; const int bh = lat ? (u >> 4) : (u - 2048), qb = lat ? (u & 15) : 0, b = bh >> 4, h = bh & 15;
;         const int row0 = lat ? b * 4096 + qb * 256 : NLAT + b * 256;
;         const att::QLoadMLA QL{QPRE + (size_t)row0 * 1536 + h * 96, RQ + row0, gq, lat ? ropeA + (size_t)(qb * 256) * 16 : nullptr};
;         const bf16* Kp = MK + (size_t)bh * NKEYS * 96; const bf16* Vp = MV + (size_t)bh * NKEYS * 64;
;         bf16* Op = AO + (size_t)row0 * 1024 + h * 64;
;         if (!use_off) att::body_dma<96, 64, false>(QL, Kp, Kp + 256 * 96, 96, Vp, Vp + 256 * 64, 64, Op, 1024, lat ? NKEYS : 256, 0.f, (char*)F.lds, F.tid);
.LBB0_1497:
	s_add_i32 s80, s77, s52
	s_cmpk_ge_i32 s80, 0x800
	s_cbranch_scc1 .Lpf_m_skip
	s_ashr_i32 s78, s80, 4
	s_mul_i32 s82, s78, 0xcc000
	s_mul_hi_i32 s83, s78, 0xcc000
	s_add_u32 s82, s65, s82
	s_addc_u32 s83, s66, s83
	s_mul_i32 s84, s78, 0x88000
	s_mul_hi_i32 s85, s78, 0x88000
	s_add_u32 s84, s74, s84
	s_addc_u32 s85, s75, s85
	v_readlane_b32 s80, v251, 12
	v_mbcnt_lo_u32_b32 v240, -1, 0
	v_mbcnt_hi_u32_b32 v240, -1, v240
	v_add_u32_e32 v240, s80, v240
	v_lshlrev_b32_e32 v241, 7, v240
	global_load_dword v242, v241, s[82:83]
	global_load_dword v243, v241, s[84:85]
